# v6
# speedup vs baseline: 1.0140x; 1.0079x over previous
.LBB0_40:
	s_lshl_b32 s12, s30, 2
	s_add_u32 s8, s16, s12
	s_addc_u32 s9, s17, 0
	s_waitcnt vmcnt(13)
	v_lshlrev_b32_e32 v42, 4, v209
	s_add_u32 s12, s18, s12
	s_addc_u32 s13, s19, 0
	global_load_dwordx4 v[38:41], v42, s[8:9]
	global_load_dwordx4 v[34:37], v42, s[12:13]
	s_lshl_b32 s36, s27, 3
	s_add_i32 s36, s36, s31
	s_mul_i32 s37, s36, 0x210
	s_add_i32 s37, s37, 0x23440
	s_mov_b32 s14, 0xaaaaaaaa
	s_mov_b32 s15, 0xaaaaaaaa
	s_mov_b32 s24, 0xcccccccc
	s_mov_b32 s25, 0xcccccccc
	v_mov_b32_e32 v42, v218
	s_nop 1
	v_max_f32_dpp v42, v42, v42 quad_perm:[1,0,3,2] row_mask:0xf bank_mask:0xf
	s_nop 1
	v_max_f32_dpp v42, v42, v42 quad_perm:[2,3,0,1] row_mask:0xf bank_mask:0xf
	s_nop 1
	v_max_f32_dpp v42, v42, v42 row_half_mirror row_mask:0xf bank_mask:0xf
	s_nop 1
	v_max_f32_dpp v42, v42, v42 row_mirror row_mask:0xf bank_mask:0xf
	v_sub_f32_e32 v44, v218, v42
	v_exp_f32_e32 v44, v44
	v_and_b32_e32 v47, 3, v131
	v_lshl_add_u32 v47, v47, 2, v203
	v_mul_f32_e32 v43, v219, v44
	v_pk_mul_f32 v[48:49], v[198:199], v[44:45] op_sel_hi:[1,0]
	v_pk_mul_f32 v[50:51], v[196:197], v[44:45] op_sel_hi:[1,0]
	v_pk_mul_f32 v[52:53], v[194:195], v[44:45] op_sel_hi:[1,0]
	v_pk_mul_f32 v[54:55], v[192:193], v[44:45] op_sel_hi:[1,0]
	v_pk_mul_f32 v[56:57], v[190:191], v[44:45] op_sel_hi:[1,0]
	v_pk_mul_f32 v[58:59], v[188:189], v[44:45] op_sel_hi:[1,0]
	v_pk_mul_f32 v[60:61], v[186:187], v[44:45] op_sel_hi:[1,0]
	v_pk_mul_f32 v[62:63], v[184:185], v[44:45] op_sel_hi:[1,0]
	v_pk_mul_f32 v[64:65], v[182:183], v[44:45] op_sel_hi:[1,0]
	v_pk_mul_f32 v[66:67], v[180:181], v[44:45] op_sel_hi:[1,0]
	v_pk_mul_f32 v[68:69], v[178:179], v[44:45] op_sel_hi:[1,0]
	v_pk_mul_f32 v[70:71], v[168:169], v[44:45] op_sel_hi:[1,0]
	v_pk_mul_f32 v[72:73], v[150:151], v[44:45] op_sel_hi:[1,0]
	v_pk_mul_f32 v[74:75], v[140:141], v[44:45] op_sel_hi:[1,0]
	v_pk_mul_f32 v[76:77], v[138:139], v[44:45] op_sel_hi:[1,0]
	v_pk_mul_f32 v[78:79], v[136:137], v[44:45] op_sel_hi:[1,0]
	v_add_u32_e32 v47, s37, v47
	v_add_f32_dpp v43, v43, v43 row_shr:1 row_mask:0xf bank_mask:0xf
	v_cndmask_b32_e64 v80, v48, v49, s[14:15]
	v_cndmask_b32_e64 v49, v49, v48, s[14:15]
	v_cndmask_b32_e64 v81, v50, v51, s[14:15]
	v_cndmask_b32_e64 v51, v51, v50, s[14:15]
	v_cndmask_b32_e64 v82, v52, v53, s[14:15]
	v_cndmask_b32_e64 v53, v53, v52, s[14:15]
	v_cndmask_b32_e64 v83, v54, v55, s[14:15]
	v_cndmask_b32_e64 v55, v55, v54, s[14:15]
	v_cndmask_b32_e64 v84, v56, v57, s[14:15]
	v_cndmask_b32_e64 v57, v57, v56, s[14:15]
	v_cndmask_b32_e64 v85, v58, v59, s[14:15]
	v_cndmask_b32_e64 v59, v59, v58, s[14:15]
	v_cndmask_b32_e64 v86, v60, v61, s[14:15]
	v_cndmask_b32_e64 v61, v61, v60, s[14:15]
	v_cndmask_b32_e64 v87, v62, v63, s[14:15]
	v_cndmask_b32_e64 v63, v63, v62, s[14:15]
	v_cndmask_b32_e64 v88, v64, v65, s[14:15]
	v_cndmask_b32_e64 v65, v65, v64, s[14:15]
	v_cndmask_b32_e64 v89, v66, v67, s[14:15]
	v_cndmask_b32_e64 v67, v67, v66, s[14:15]
	v_cndmask_b32_e64 v90, v68, v69, s[14:15]
	v_cndmask_b32_e64 v69, v69, v68, s[14:15]
	v_cndmask_b32_e64 v91, v70, v71, s[14:15]
	v_cndmask_b32_e64 v71, v71, v70, s[14:15]
	v_cndmask_b32_e64 v92, v72, v73, s[14:15]
	v_cndmask_b32_e64 v73, v73, v72, s[14:15]
	v_cndmask_b32_e64 v93, v74, v75, s[14:15]
	v_cndmask_b32_e64 v75, v75, v74, s[14:15]
	v_cndmask_b32_e64 v94, v76, v77, s[14:15]
	v_cndmask_b32_e64 v77, v77, v76, s[14:15]
	v_cndmask_b32_e64 v95, v78, v79, s[14:15]
	v_cndmask_b32_e64 v79, v79, v78, s[14:15]
	v_add_f32_dpp v43, v43, v43 row_shr:2 row_mask:0xf bank_mask:0xf
	v_add_f32_dpp v48, v49, v80 quad_perm:[1,0,3,2] row_mask:0xf bank_mask:0xf
	v_add_f32_dpp v50, v51, v81 quad_perm:[1,0,3,2] row_mask:0xf bank_mask:0xf
	v_add_f32_dpp v52, v53, v82 quad_perm:[1,0,3,2] row_mask:0xf bank_mask:0xf
	v_add_f32_dpp v54, v55, v83 quad_perm:[1,0,3,2] row_mask:0xf bank_mask:0xf
	v_add_f32_dpp v56, v57, v84 quad_perm:[1,0,3,2] row_mask:0xf bank_mask:0xf
	v_add_f32_dpp v58, v59, v85 quad_perm:[1,0,3,2] row_mask:0xf bank_mask:0xf
	v_add_f32_dpp v60, v61, v86 quad_perm:[1,0,3,2] row_mask:0xf bank_mask:0xf
	v_add_f32_dpp v62, v63, v87 quad_perm:[1,0,3,2] row_mask:0xf bank_mask:0xf
	v_add_f32_dpp v64, v65, v88 quad_perm:[1,0,3,2] row_mask:0xf bank_mask:0xf
	v_add_f32_dpp v66, v67, v89 quad_perm:[1,0,3,2] row_mask:0xf bank_mask:0xf
	v_add_f32_dpp v68, v69, v90 quad_perm:[1,0,3,2] row_mask:0xf bank_mask:0xf
	v_add_f32_dpp v70, v71, v91 quad_perm:[1,0,3,2] row_mask:0xf bank_mask:0xf
	v_add_f32_dpp v72, v73, v92 quad_perm:[1,0,3,2] row_mask:0xf bank_mask:0xf
	v_add_f32_dpp v74, v75, v93 quad_perm:[1,0,3,2] row_mask:0xf bank_mask:0xf
	v_add_f32_dpp v76, v77, v94 quad_perm:[1,0,3,2] row_mask:0xf bank_mask:0xf
	v_add_f32_dpp v78, v79, v95 quad_perm:[1,0,3,2] row_mask:0xf bank_mask:0xf
	v_add_f32_dpp v43, v43, v43 row_shr:4 row_mask:0xf bank_mask:0xf
	v_cndmask_b32_e64 v80, v48, v50, s[24:25]
	v_cndmask_b32_e64 v50, v50, v48, s[24:25]
	v_cndmask_b32_e64 v81, v52, v54, s[24:25]
	v_cndmask_b32_e64 v54, v54, v52, s[24:25]
	v_cndmask_b32_e64 v82, v56, v58, s[24:25]
	v_cndmask_b32_e64 v58, v58, v56, s[24:25]
	v_cndmask_b32_e64 v83, v60, v62, s[24:25]
	v_cndmask_b32_e64 v62, v62, v60, s[24:25]
	v_cndmask_b32_e64 v84, v64, v66, s[24:25]
	v_cndmask_b32_e64 v66, v66, v64, s[24:25]
	v_cndmask_b32_e64 v85, v68, v70, s[24:25]
	v_cndmask_b32_e64 v70, v70, v68, s[24:25]
	v_cndmask_b32_e64 v86, v72, v74, s[24:25]
	v_cndmask_b32_e64 v74, v74, v72, s[24:25]
	v_cndmask_b32_e64 v87, v76, v78, s[24:25]
	v_cndmask_b32_e64 v78, v78, v76, s[24:25]
	v_add_f32_dpp v43, v43, v43 row_shr:8 row_mask:0xf bank_mask:0xf
	v_add_f32_dpp v48, v50, v80 quad_perm:[2,3,0,1] row_mask:0xf bank_mask:0xf
	v_add_f32_dpp v52, v54, v81 quad_perm:[2,3,0,1] row_mask:0xf bank_mask:0xf
	v_add_f32_dpp v56, v58, v82 quad_perm:[2,3,0,1] row_mask:0xf bank_mask:0xf
	v_add_f32_dpp v60, v62, v83 quad_perm:[2,3,0,1] row_mask:0xf bank_mask:0xf
	v_add_f32_dpp v64, v66, v84 quad_perm:[2,3,0,1] row_mask:0xf bank_mask:0xf
	v_add_f32_dpp v68, v70, v85 quad_perm:[2,3,0,1] row_mask:0xf bank_mask:0xf
	v_add_f32_dpp v72, v74, v86 quad_perm:[2,3,0,1] row_mask:0xf bank_mask:0xf
	v_add_f32_dpp v76, v78, v87 quad_perm:[2,3,0,1] row_mask:0xf bank_mask:0xf
	v_add_f32_dpp v48, v48, v48 row_shr:4 row_mask:0xf bank_mask:0xf
	v_add_f32_dpp v52, v52, v52 row_shr:4 row_mask:0xf bank_mask:0xf
	v_add_f32_dpp v56, v56, v56 row_shr:4 row_mask:0xf bank_mask:0xf
	v_add_f32_dpp v60, v60, v60 row_shr:4 row_mask:0xf bank_mask:0xf
	v_add_f32_dpp v64, v64, v64 row_shr:4 row_mask:0xf bank_mask:0xf
	v_add_f32_dpp v68, v68, v68 row_shr:4 row_mask:0xf bank_mask:0xf
	v_add_f32_dpp v72, v72, v72 row_shr:4 row_mask:0xf bank_mask:0xf
	v_add_f32_dpp v76, v76, v76 row_shr:4 row_mask:0xf bank_mask:0xf
	v_add_f32_dpp v48, v48, v48 row_shr:8 row_mask:0xf bank_mask:0xf
	v_add_f32_dpp v52, v52, v52 row_shr:8 row_mask:0xf bank_mask:0xf
	v_add_f32_dpp v56, v56, v56 row_shr:8 row_mask:0xf bank_mask:0xf
	v_add_f32_dpp v60, v60, v60 row_shr:8 row_mask:0xf bank_mask:0xf
	v_add_f32_dpp v64, v64, v64 row_shr:8 row_mask:0xf bank_mask:0xf
	v_add_f32_dpp v68, v68, v68 row_shr:8 row_mask:0xf bank_mask:0xf
	v_add_f32_dpp v72, v72, v72 row_shr:8 row_mask:0xf bank_mask:0xf
	v_add_f32_dpp v76, v76, v76 row_shr:8 row_mask:0xf bank_mask:0xf
	s_mov_b64 s[28:29], exec
	s_mov_b32 exec_lo, 0xf000f000
	s_mov_b32 exec_hi, 0xf000f000
	ds_write_b32 v47, v48
	ds_write_b32 v47, v52 offset:64
	ds_write_b32 v47, v56 offset:128
	ds_write_b32 v47, v60 offset:192
	ds_write_b32 v47, v64 offset:256
	ds_write_b32 v47, v68 offset:320
	ds_write_b32 v47, v72 offset:384
	ds_write_b32 v47, v76 offset:448
	s_mov_b64 exec, s[4:5]
	v_mov_b32_e32 v44, s37
	ds_write_b64 v44, v[42:43] offset:512
	s_mov_b64 exec, s[28:29]
	v_lshrrev_b32_e32 v42, 7, v0
	s_movk_i32 s4, 0x1080
	v_mov_b32_e32 v43, 0x23440
	s_waitcnt vmcnt(11)
	v_mad_u32_u24 v59, v42, s4, v43
	s_load_dword s6, s[22:23], 0x0
	s_waitcnt lgkmcnt(0)
	s_barrier
	ds_read_b32 v46, v59 offset:512
	ds_read_b32 v47, v59 offset:1040
	ds_read_b32 v50, v59 offset:1568
	ds_read_b32 v51, v59 offset:2096
	ds_read_b64 v[42:43], v59 offset:1040
	ds_read_b64 v[44:45], v59 offset:512
	s_mov_b32 s4, 0xff800000
	s_waitcnt vmcnt(8)
	v_cvt_pk_bf16_f32 v30, v30, v31
	v_cvt_pk_bf16_f32 v31, v32, v33
	s_waitcnt lgkmcnt(4)
	v_max3_f32 v52, v46, s4, v47
	ds_read_b64 v[46:47], v59 offset:2096
	ds_read_b64 v[48:49], v59 offset:1568
	s_waitcnt lgkmcnt(4)
	v_max3_f32 v54, v52, v50, v51
	ds_read_b32 v55, v59 offset:2624
	ds_read_b32 v56, v59 offset:3152
	ds_read_b32 v58, v59 offset:3680
	ds_read_b32 v60, v59 offset:4208
	ds_read_b64 v[50:51], v59 offset:3152
	ds_read_b64 v[52:53], v59 offset:2624
	s_waitcnt lgkmcnt(4)
	v_max3_f32 v61, v54, v55, v56
	ds_read_b64 v[54:55], v59 offset:4208
	ds_read_b64 v[56:57], v59 offset:3680
	s_waitcnt lgkmcnt(4)
	v_max3_f32 v63, v61, v58, v60
	v_and_b32_e32 v60, 0x1fc, v130
	v_sub_f32_e32 v44, v44, v63
	v_sub_f32_e32 v42, v42, v63
	v_exp_f32_e32 v58, v44
	v_add_u32_e32 v44, v59, v60
	v_exp_f32_e32 v62, v42
	v_sub_f32_e32 v42, v48, v63
	v_exp_f32_e32 v64, v42
	v_add_u32_e32 v42, 0x400, v44
	ds_read2_b32 v[66:67], v42 offset0:8 offset1:140
	v_sub_f32_e32 v42, v46, v63
	ds_read2_b32 v[60:61], v44 offset1:132
	v_exp_f32_e32 v68, v42
	s_waitcnt lgkmcnt(4)
	v_sub_f32_e32 v42, v52, v63
	v_exp_f32_e32 v70, v42
	v_add_u32_e32 v42, 0x800, v44
	ds_read2_b32 v[72:73], v42 offset0:16 offset1:148
	v_sub_f32_e32 v42, v50, v63
	s_waitcnt vmcnt(7)
	v_exp_f32_e32 v74, v42
	s_waitcnt lgkmcnt(3)
	v_sub_f32_e32 v42, v56, v63
	v_exp_f32_e32 v76, v42
	v_add_u32_e32 v42, 0xc00, v44
	s_waitcnt vmcnt(6)
	ds_read2_b32 v[78:79], v42 offset0:24 offset1:156
	v_sub_f32_e32 v42, v54, v63
	s_waitcnt lgkmcnt(2)
	v_mov_b32_e32 v44, v60
	v_exp_f32_e32 v80, v42
	v_pk_fma_f32 v[44:45], v[44:45], v[58:59], 0 op_sel_hi:[1,0,0]
	v_mov_b32_e32 v42, v61
	v_pk_fma_f32 v[42:43], v[42:43], v[62:63], v[44:45] op_sel_hi:[1,0,1]
	v_mov_b32_e32 v48, v66
	v_pk_fma_f32 v[42:43], v[48:49], v[64:65], v[42:43] op_sel_hi:[1,0,1]
	v_mov_b32_e32 v46, v67
	v_pk_fma_f32 v[42:43], v[46:47], v[68:69], v[42:43] op_sel_hi:[1,0,1]
	s_waitcnt lgkmcnt(1)
	v_mov_b32_e32 v52, v72
	v_pk_fma_f32 v[42:43], v[52:53], v[70:71], v[42:43] op_sel_hi:[1,0,1]
	v_mov_b32_e32 v50, v73
	v_pk_fma_f32 v[42:43], v[50:51], v[74:75], v[42:43] op_sel_hi:[1,0,1]
	s_waitcnt lgkmcnt(0)
	v_mov_b32_e32 v56, v78
	v_pk_fma_f32 v[42:43], v[56:57], v[76:77], v[42:43] op_sel_hi:[1,0,1]
	v_mov_b32_e32 v54, v79
	v_pk_fma_f32 v[42:43], v[54:55], v[80:81], v[42:43] op_sel_hi:[1,0,1]
	v_cvt_pk_bf16_f32 v32, v26, v27
	v_div_scale_f32 v44, s[4:5], v43, v43, v42
	v_rcp_f32_e32 v45, v44
	s_movk_i32 s4, 0x600
	v_cvt_pk_bf16_f32 v33, v28, v29
	v_cvt_pk_bf16_f32 v22, v22, v23
	v_fma_f32 v46, -v44, v45, 1.0
	v_fmac_f32_e32 v45, v46, v45
	v_div_scale_f32 v46, vcc, v42, v43, v42
	v_mul_f32_e32 v47, v46, v45
	v_fma_f32 v48, -v44, v47, v46
	v_fmac_f32_e32 v47, v48, v45
	v_fma_f32 v44, -v44, v47, v46
	v_div_fmas_f32 v44, v44, v45, v47
	v_div_fixup_f32 v42, v44, v43, v42
	v_fma_f32 v42, v42, -2.0, 1.0
	v_add_u32_e32 v43, 0x22400, v130
	ds_write_b32 v43, v42
	v_lshlrev_b32_e32 v42, 9, v0
	v_and_or_b32 v42, v42, s4, v132
	v_add_u32_e32 v50, 0x22400, v42
	s_waitcnt lgkmcnt(0)
	s_barrier
	ds_read_b128 v[42:45], v50
	ds_read_b128 v[46:49], v50 offset:16
	v_cvt_pk_bf16_f32 v23, v24, v25
	v_cvt_pk_bf16_f32 v24, v18, v19
	v_cvt_pk_bf16_f32 v25, v20, v21
	s_waitcnt lgkmcnt(1)
	v_cvt_pk_bf16_f32 v26, v42, v43
	v_cvt_pk_bf16_f32 v27, v44, v45
	s_waitcnt lgkmcnt(0)
	v_cvt_pk_bf16_f32 v28, v46, v47
	v_cvt_pk_bf16_f32 v29, v48, v49
	ds_read_b128 v[42:45], v50 offset:144
	s_waitcnt vmcnt(4)
	v_cvt_pk_bf16_f32 v14, v14, v15
	v_mfma_f32_16x16x32_bf16 v[26:29], v[30:33], v[26:29], 0
	ds_read_b128 v[30:33], v50 offset:128
	v_cvt_pk_bf16_f32 v15, v16, v17
	s_waitcnt lgkmcnt(1)
	v_cvt_pk_bf16_f32 v20, v42, v43
	v_cvt_pk_bf16_f32 v21, v44, v45
	v_cvt_pk_bf16_f32 v16, v10, v11
	s_waitcnt lgkmcnt(0)
	v_cvt_pk_bf16_f32 v18, v30, v31
	v_cvt_pk_bf16_f32 v19, v32, v33
	v_cvt_pk_bf16_f32 v17, v12, v13
	s_waitcnt vmcnt(2)
	v_cvt_pk_bf16_f32 v6, v6, v7
	v_mfma_f32_16x16x32_bf16 v[18:21], v[22:25], v[18:21], v[26:29]
	ds_read_b128 v[22:25], v50 offset:256
	v_cvt_pk_bf16_f32 v7, v8, v9
	v_cvt_pk_bf16_f32 v8, v2, v3
	ds_read_b128 v[26:29], v50 offset:272
	v_cvt_pk_bf16_f32 v9, v4, v5
	s_waitcnt lgkmcnt(1)
	v_cvt_pk_bf16_f32 v10, v22, v23
	v_cvt_pk_bf16_f32 v11, v24, v25
	s_mov_b32 s4, 0x3f200000
	s_waitcnt lgkmcnt(0)
	v_cvt_pk_bf16_f32 v12, v26, v27
	v_cvt_pk_bf16_f32 v13, v28, v29
	s_nop 1
	v_mfma_f32_16x16x32_bf16 v[10:13], v[14:17], v[10:13], v[18:21]
	ds_read_b128 v[14:17], v50 offset:384
	s_nop 1
	ds_read_b128 v[18:21], v50 offset:400
	s_waitcnt lgkmcnt(1)
	v_cvt_pk_bf16_f32 v2, v14, v15
	v_cvt_pk_bf16_f32 v3, v16, v17
	s_waitcnt lgkmcnt(0)
	v_cvt_pk_bf16_f32 v4, v18, v19
	v_cvt_pk_bf16_f32 v5, v20, v21
	s_nop 1
	v_mfma_f32_16x16x32_bf16 v[2:5], v[6:9], v[2:5], v[10:13]
	s_waitcnt vmcnt(1)
	s_nop 6
	v_add_f32_e32 v2, v2, v38
	v_cmp_nlt_f32_e64 s[4:5], |v2|, s4
	s_and_saveexec_b64 s[8:9], s[4:5]
	s_xor_b64 s[4:5], exec, s[8:9]
	s_cbranch_execz .LBB0_60
	v_add_f32_e64 v6, |v2|, |v2|
	v_mul_f32_e32 v7, 0x3fb8aa3b, v6
	s_mov_b32 s7, 0x3fb8aa3b
	v_rndne_f32_e32 v8, v7
	v_sub_f32_e32 v9, v7, v8
	v_fma_f32 v7, v6, s7, -v7
	v_fmamk_f32 v7, v6, 0x32a5705f, v7
	v_add_f32_e32 v7, v9, v7
	v_exp_f32_e32 v7, v7
	v_cvt_i32_f32_e32 v8, v8
	s_mov_b32 s7, 0xc2ce8ed0
	v_cmp_ngt_f32_e32 vcc, s7, v6
	s_mov_b32 s7, 0x42b17218
	v_ldexp_f32 v7, v7, v8
	v_cndmask_b32_e32 v7, 0, v7, vcc
	v_mov_b32_e32 v8, 0x7f800000
	v_cmp_nlt_f32_e32 vcc, s7, v6
	s_nop 1
	v_cndmask_b32_e32 v6, v8, v7, vcc
	v_add_f32_e32 v6, 1.0, v6
	v_rcp_f32_e32 v6, v6
	s_nop 0
	v_fma_f32 v6, v6, -2.0, 1.0
